# fused P7->P8 hand-off inside an XCD: per-wave progress words for finished gate/up units, down-projection units wait only for the 8 workgroups that produced their row tile; P8 ranks rotated by 16; no b
# speedup vs baseline: 1.0164x; 1.0125x over previous
.LBB0_1220:
	s_cmp_eq_u32 s96, 0
	s_cbranch_scc1 .Lp7pub_skip
	v_readlane_b32 s28, v255, 9
	v_readlane_b32 s29, v255, 10
	v_readlane_b32 s30, v255, 8
	v_readlane_b32 s31, v255, 18
	s_lshl_b32 s0, s30, 5
	s_lshl_b32 s31, s31, 2
	s_add_i32 s0, s0, s31
	s_add_i32 s0, s0, 0x4000
	s_mov_b64 s[60:61], exec
	s_mov_b64 exec, 1
	v_mov_b32_e32 v2, s0
	v_mov_b32_e32 v5, 1
	global_atomic_add v2, v5, s[28:29]
	s_mov_b64 exec, s[60:61]

.LBB0_1232:
	s_cmp_gt_i32 s81, 8
	s_cselect_b64 s[0:1], -1, 0
	s_and_b64 s[2:3], s[12:13], s[0:1]
	s_andn2_b64 vcc, exec, s[2:3]
	s_cbranch_vccnz .LBB0_1284
	s_waitcnt vmcnt(0)
	s_waitcnt vmcnt(0) lgkmcnt(0)
	v_readlane_b32 s6, v255, 9
	v_readlane_b32 s7, v255, 10
	v_readlane_b32 s9, v255, 8
	v_readlane_b32 s14, v255, 18
	s_lshl_b32 s8, s9, 5
	s_lshl_b32 s14, s14, 2
	s_add_i32 s8, s8, s14
	s_add_i32 s8, s8, 0x4000
	s_mov_b64 s[16:17], exec
	s_mov_b64 exec, 1
	v_mov_b32_e32 v2, s8
	v_mov_b32_e32 v4, 1
	global_atomic_add v2, v4, s[6:7]
	s_mov_b64 exec, s[16:17]
	s_barrier
	s_mov_b64 s[4:5], exec
	v_readlane_b32 s2, v255, 12
	v_readlane_b32 s3, v255, 13
	s_and_b64 s[2:3], s[4:5], s[2:3]
	s_mov_b64 exec, s[2:3]
	s_cbranch_execz .LBB0_1283
	v_readlane_b32 s8, v255, 11
	v_readlane_b32 s12, v255, 9
	v_readlane_b32 s13, v255, 10
	v_mov_b32_e32 v4, 0x20160
	ds_read_b32 v4, v4
	s_lshl_b32 s8, s8, 8
	s_add_u32 s8, s12, s8
	s_addc_u32 s9, s13, 0
	v_mov_b32_e32 v5, 0x2000
	v_mov_b32_e32 v6, 1
	v_mov_b32_e32 v2, 0x3000
	s_mov_b32 s2, 0
	global_atomic_add v5, v6, s[8:9] offset:1024
	buffer_inv sc1
	global_load_dword v2, v2, s[12:13] offset:896 sc1
	s_waitcnt lgkmcnt(0)
	v_mul_u32_u24_e32 v4, 3, v4
.Lxl_spin_2:
	global_load_dword v6, v5, s[8:9] offset:1024 sc1
	s_waitcnt vmcnt(0)
	v_cmp_ne_u32_e32 vcc, 0, v2
	s_cbranch_vccnz .Lxl_full_2
	s_branch .LBB0_1283

.LBB0_1284:
	s_cmp_lt_i32 s80, 9
	s_cselect_b64 s[2:3], -1, 0
	s_add_u32 s12, s90, 0x11000000
	s_addc_u32 s13, s91, 0
	s_and_b64 s[14:15], s[2:3], s[0:1]
	s_andn2_b64 vcc, exec, s[14:15]
	s_cbranch_vccnz .LBB0_1341
	s_mov_b32 s32, 0
	v_readlane_b32 s2, v255, 2
	s_cmpk_lg_i32 s2, 0x100
	s_cbranch_scc1 .Lp8done_f
	v_readlane_b32 s33, v255, 8
	s_and_b32 s33, s33, 31
	s_xor_b32 s33, s33, 16
	s_lshr_b32 s2, s33, 4
	s_add_i32 s2, s2, 1
	v_readlane_b32 s28, v255, 9
	v_readlane_b32 s29, v255, 10
	v_readlane_b32 s3, v255, 8
	s_lshr_b32 s3, s3, 5
	s_lshl_b32 s3, s3, 10
	s_lshr_b32 s4, s33, 2
	s_and_b32 s4, s4, 3
	s_lshl_b32 s4, s4, 8
	s_add_i32 s3, s3, s4
	s_add_i32 s3, s3, 0x4000
	v_mbcnt_lo_u32_b32 v240, -1, 0
	v_mbcnt_hi_u32_b32 v240, -1, v240
	v_lshlrev_b32_e32 v240, 2, v240
	v_add_u32_e32 v240, s3, v240
	s_mov_b32 s5, 0
.Lp8spin_f:
	global_load_dword v241, v240, s[28:29] sc1
	s_waitcnt vmcnt(0)
	v_cmp_le_u32_e32 vcc, s2, v241
	s_cmp_eq_u64 vcc, exec
	s_cbranch_scc1 .Lp8ready_f
	s_sleep 4
	s_add_u32 s5, s5, 1
	s_cmp_lt_u32 s5, 0x1000
	s_cbranch_scc1 .Lp8spin_f
.Lp8ready_f:
	s_mov_b32 s32, s2
.Lp8raise_f:
	s_add_i32 s3, s32, 1
	v_cmp_le_u32_e32 vcc, s3, v241
	s_cmp_eq_u64 vcc, exec
	s_cbranch_scc0 .Lp8done_f
	s_mov_b32 s32, s3
	s_cmp_lt_u32 s32, 16
	s_cbranch_scc1 .Lp8raise_f
.Lp8done_f:
	s_add_i32 s1, 0, 0x20510
	s_movk_i32 s0, 0x200
	v_mov_b32_e32 v2, s1
	ds_read_b32 v2, v2
	s_ashr_i32 s33, s89, 3
	v_readlane_b32 s8, v255, 2
	s_cmpk_lg_i32 s8, 0x100
	s_cbranch_scc1 .Lp8rot_skip
	s_xor_b32 s33, s33, 16
.Lp8rot_skip:
	s_and_b32 s6, s89, 7
	v_readfirstlane_b32 s7, v0
	s_and_b64 vcc, exec, s[26:27]
	s_waitcnt lgkmcnt(0)
	v_readfirstlane_b32 s1, v2
	s_lshl_b32 s34, s1, 2
	s_mov_b64 s[2:3], -1
	s_cbranch_vccnz .LBB0_1288
	s_add_i32 s1, s34, 31
	s_ashr_i32 s1, s1, 5
	s_lshl_b32 s1, s1, 2
	s_cmp_lt_i32 s33, s1
	s_cbranch_scc0 .LBB0_1292
	s_mul_i32 s1, s1, s6
	s_add_i32 s1, s1, s33
	v_writelane_b32 v255, s1, 7

.LBB0_1307:
	s_mov_b64 s[0:1], -1
	s_and_b64 vcc, exec, s[2:3]
	s_cbranch_vccz .LBB0_1310
	s_cmp_ge_i32 s4, s34
	s_cbranch_scc1 .LBB0_1310
	v_readlane_b32 s0, v255, 2
	s_cmpk_lg_i32 s0, 0x100
	s_cbranch_scc1 .Lp8done_n
	s_lshr_b32 s0, s33, 4
	s_lshl_b32 s1, s74, 1
	s_add_i32 s0, s0, s1
	s_add_i32 s0, s0, 1
	s_cmp_le_u32 s0, s32
	s_cbranch_scc1 .Lp8done_n
	v_readlane_b32 s28, v255, 9
	v_readlane_b32 s29, v255, 10
	v_readlane_b32 s1, v255, 8
	s_lshr_b32 s1, s1, 5
	s_lshl_b32 s1, s1, 10
	s_lshr_b32 s2, s33, 2
	s_and_b32 s2, s2, 3
	s_lshl_b32 s2, s2, 8
	s_add_i32 s1, s1, s2
	s_add_i32 s1, s1, 0x4000
	v_mbcnt_lo_u32_b32 v0, -1, 0
	v_mbcnt_hi_u32_b32 v0, -1, v0
	v_lshlrev_b32_e32 v0, 2, v0
	v_add_u32_e32 v0, s1, v0
	s_mov_b32 s3, 0
.Lp8spin_n:
	global_load_dword v2, v0, s[28:29] sc1
	s_waitcnt vmcnt(0)
	v_cmp_le_u32_e32 vcc, s0, v2
	s_cmp_eq_u64 vcc, exec
	s_cbranch_scc1 .Lp8ready_n
	s_sleep 4
	s_add_u32 s3, s3, 1
	s_cmp_lt_u32 s3, 0x1000
	s_cbranch_scc1 .Lp8spin_n
.Lp8ready_n:
	s_mov_b32 s32, s0
.Lp8raise_n:
	s_add_i32 s1, s32, 1
	v_cmp_le_u32_e32 vcc, s1, v2
	s_cmp_eq_u64 vcc, exec
	s_cbranch_scc0 .Lp8done_n
	s_mov_b32 s32, s1
	s_cmp_lt_u32 s32, 16
	s_cbranch_scc1 .Lp8raise_n
.Lp8done_n:
	s_ashr_i32 s0, s4, 31
	s_lshr_b32 s0, s0, 30
	s_add_i32 s0, s4, s0
	s_ashr_i32 s0, s0, 2
	v_mbcnt_lo_u32_b32 v0, -1, 0
	v_mbcnt_hi_u32_b32 v0, -1, v0
	v_min_u32_e32 v0, 32, v0
	v_lshlrev_b32_e32 v0, 2, v0
	v_add_u32_e32 v2, 0x20400, v0
	v_add_u32_e32 v0, 0x20490, v0
	ds_read_b32 v2, v2
	ds_read_b32 v0, v0
	s_waitcnt lgkmcnt(0)
	v_cmp_ge_i32_e32 vcc, s0, v0
	s_and_b32 s46, vcc_lo, 0xfffffffe
	s_bcnt1_i32_b32 s46, s46
	s_add_i32 s2, s46, 1
	v_readlane_b32 s1, v0, s46
	v_readlane_b32 s3, v2, s2
	v_readlane_b32 s2, v2, s46
	s_sub_i32 s1, s0, s1
	s_lshl_b32 s1, s1, 8
	s_add_i32 s80, s2, s1
	s_sub_i32 s1, s3, s80
	s_sub_i32 s0, s46, s0
	s_min_i32 s79, s1, 0x100
	s_lshl_b32 s0, s0, 10
	s_lshl_b32 s1, s4, 8
	s_add_i32 s63, s0, s1
	s_mov_b64 s[0:1], 0
